# attention: far-bucket test list reads prefetched at loop top (no LDS round trip per step); on top of v14
# speedup vs baseline: 1.0065x; 1.0065x over previous
.LBB0_720:
	s_add_i32 s12, s47, -2
	s_lshr_b32 s42, s12, 2
	s_add_i32 s42, s42, s44
	s_and_b32 s34, s12, 2
	s_lshl_b32 s12, s42, 9
	s_add_i32 s43, s12, 0
	s_lshl_b32 s12, s34, 7
	s_add_i32 s43, s43, s12
	v_mov_b32_e32 v200, s43
	ds_read_u16 v201, v200 offset:33022
	ds_read_u16 v200, v200 offset:32894
	v_lshl_add_u32 v90, v233, 1, s43
	ds_read_u16 v102, v90 offset:32896
	ds_read_u16 v106, v90 offset:32912
	ds_read_u16 v110, v90 offset:32928
	ds_read_u16 v114, v90 offset:32944
	ds_read_u16 v86, v90 offset:32960
	ds_read_u16 v91, v90 offset:32976
	ds_read_u16 v94, v90 offset:32992
	ds_read_u16 v98, v90 offset:33008
	s_waitcnt lgkmcnt(7)
	v_lshlrev_b32_e32 v0, 9, v102
	v_lshl_add_u64 v[102:103], v[212:213], 0, v[0:1]
	global_load_dwordx4 v[138:141], v[102:103], off
	s_waitcnt lgkmcnt(6)
	v_lshlrev_b32_e32 v0, 9, v106
	v_lshl_add_u64 v[106:107], v[212:213], 0, v[0:1]
	global_load_dwordx4 v[142:145], v[106:107], off
	s_waitcnt lgkmcnt(5)
	v_lshlrev_b32_e32 v0, 9, v110
	v_lshl_add_u64 v[110:111], v[212:213], 0, v[0:1]
	global_load_dwordx4 v[146:149], v[110:111], off
	s_waitcnt lgkmcnt(4)
	v_lshlrev_b32_e32 v0, 9, v114
	v_lshl_add_u64 v[114:115], v[212:213], 0, v[0:1]
	global_load_dwordx4 v[134:137], v[114:115], off
	s_waitcnt lgkmcnt(3)
	v_lshlrev_b32_e32 v0, 9, v86
	v_lshl_add_u64 v[86:87], v[212:213], 0, v[0:1]
	global_load_dwordx4 v[130:133], v[86:87], off
	s_waitcnt lgkmcnt(2)
	v_lshlrev_b32_e32 v0, 9, v91
	v_lshl_add_u64 v[90:91], v[212:213], 0, v[0:1]
	global_load_dwordx4 v[126:129], v[90:91], off
	s_waitcnt lgkmcnt(1)
	v_lshlrev_b32_e32 v0, 9, v94
	v_lshl_add_u64 v[94:95], v[212:213], 0, v[0:1]
	global_load_dwordx4 v[122:125], v[94:95], off
	s_waitcnt lgkmcnt(0)
	v_lshlrev_b32_e32 v0, 9, v98
	v_lshl_add_u64 v[98:99], v[212:213], 0, v[0:1]
	global_load_dwordx4 v[118:121], v[98:99], off
	global_load_dwordx4 v[102:105], v[102:103], off offset:128
	s_nop 0
	global_load_dwordx4 v[106:109], v[106:107], off offset:128
	s_nop 0
	global_load_dwordx4 v[110:113], v[110:111], off offset:128
	s_nop 0
	global_load_dwordx4 v[114:117], v[114:115], off offset:128
	s_nop 0
	global_load_dwordx4 v[86:89], v[86:87], off offset:128
	s_nop 0
	global_load_dwordx4 v[90:93], v[90:91], off offset:128
	s_nop 0
	global_load_dwordx4 v[94:97], v[94:95], off offset:128
	s_nop 0
	global_load_dwordx4 v[98:101], v[98:99], off offset:128
	s_cmp_eq_u32 s34, 0
	s_cselect_b64 s[30:31], -1, 0
	s_cmp_lg_u32 s34, 0
	s_cbranch_scc1 .LBB0_722
	v_mov_b32_e32 v244, 0
	v_mov_b32_e32 v202, 0xf149f2ca
	v_mov_b32_e32 v154, 0
	v_mov_b32_e32 v155, v244
	v_mov_b32_e32 v156, v244
	v_mov_b32_e32 v157, v244
	v_mov_b32_e32 v158, 0
	v_mov_b32_e32 v159, v244
	v_mov_b32_e32 v160, v244
	v_mov_b32_e32 v161, v244
	v_mov_b32_e32 v162, 0
	v_mov_b32_e32 v163, v244
	v_mov_b32_e32 v164, v244
	v_mov_b32_e32 v165, v244
	v_mov_b32_e32 v166, 0
	v_mov_b32_e32 v167, v244
	v_mov_b32_e32 v168, v244
	v_mov_b32_e32 v169, v244
.LBB0_722:
	s_add_i32 s42, s42, s49
	s_cmpk_gt_i32 s42, 0xfe
	s_cselect_b64 s[40:41], -1, 0
	s_cmpk_lt_i32 s42, 0xff
	v_mov_b32_e32 v0, 0
	s_cbranch_scc1 .LBB0_724
	s_movk_i32 s12, 0x7e
	v_sub_u32_e32 v0, s42, v200
	v_cmp_lt_i32_e32 vcc, s12, v0
	s_nop 1
	v_cndmask_b32_e64 v0, 0, 1, vcc

.LBB0_746:
	s_andn2_b64 vcc, exec, s[40:41]
	v_mov_b32_e32 v0, 0
	s_cbranch_vccnz .LBB0_748
	s_movk_i32 s12, 0x7e
	v_sub_u32_e32 v0, s42, v201
	v_cmp_lt_i32_e32 vcc, s12, v0
	s_nop 1
	v_cndmask_b32_e64 v0, 0, 1, vcc
